# v23 = v20 + naprep rows assigned so 8 consecutive rows (one 128-byte line of key fragments) are written from one XCD
# baseline (speedup 1.0000x reference)
; #define NAP_LOAD(ROW) do { const bf16_t* pp_ = p.P + (size_t)(ROW) * L0LD + RWC + wave * 128 + lane; \
;         nq[0] = bf2f(pp_[0]); nq[1] = bf2f(pp_[64]); nk[0] = bf2f(pp_[1024]); nk[1] = bf2f(pp_[1088]); } while (0)
; __device__ __forceinline__ void ph_naprep(const Params& p, float* lds, int wg, int nwg) {
;     ...
;         const float kb = 8.f * wave_max(fabsf(p.in[21][lane]));
;         float bmax[2];
; #pragma unroll
;         for (int hh = 0; hh < 2; ++hh) { float m = 0.f; for (int i = lane; i < 465; i += 64) m = fmaxf(m, fabsf(p.in[22][(wave * 2 + hh) * 465 + i])); bmax[hh] = wave_max(m); }
;         const float qw = p.in[20][lane] * 0.125f, kw = p.in[21][lane];
;         float nq[2], nk[2];
;     ...
;         NAP_LOAD(wg < NT ? wg : 0);
;         for (int row = wg; row < NT; row += nwg) {
;             const float cq[2] = {nq[0], nq[1]}, ck[2] = {nk[0], nk[1]};
;             NAP_LOAD(row + nwg < NT ? row + nwg : row);
.LBB0_542:
	s_movk_i32 s2, 0x211
	v_add3_u32 v18, v15, v16, s2
	v_ashrrev_i32_e32 v19, 31, v18
	v_lshl_add_u64 v[18:19], v[18:19], 2, s[12:13]
	global_load_dword v3, v[18:19], off
	v_add_u32_e32 v16, 64, v16
	s_movk_i32 s2, 0x190
	v_max_f32_e32 v2, v2, v2
	v_cmp_lt_u32_e32 vcc, s2, v16
	s_or_b64 s[0:1], vcc, s[0:1]
	s_waitcnt vmcnt(0)
	v_max_f32_e64 v3, |v3|, |v3|
	v_max_f32_e32 v2, v2, v3
	s_andn2_b64 exec, exec, s[0:1]
	s_cbranch_execnz .LBB0_542
	s_or_b64 exec, exec, s[0:1]
	ds_bpermute_b32 v3, v165, v2
	v_max_f32_e32 v2, v2, v2
	s_cmpk_lt_i32 s90, 0x2200
	s_cselect_b64 s[34:35], -1, 0
	s_and_b64 vcc, exec, s[34:35]
	s_waitcnt lgkmcnt(0)
	v_max_f32_e32 v3, v3, v3
	v_max_f32_e32 v2, v2, v3
	ds_bpermute_b32 v3, v188, v2
	s_waitcnt lgkmcnt(0)
	v_max_f32_e32 v3, v3, v3
	v_max_f32_e32 v2, v2, v3
	ds_bpermute_b32 v3, v8, v2
	s_waitcnt lgkmcnt(0)
	v_max_f32_e32 v3, v3, v3
	v_max_f32_e32 v2, v2, v3
	ds_bpermute_b32 v3, v11, v2
	s_waitcnt lgkmcnt(0)
	v_max_f32_e32 v3, v3, v3
	v_max_f32_e32 v2, v2, v3
	ds_bpermute_b32 v3, v13, v2
	s_waitcnt lgkmcnt(0)
	v_max_f32_e32 v3, v3, v3
	v_max_f32_e32 v8, v2, v3
	ds_bpermute_b32 v11, v14, v8
	s_cbranch_vccz .LBB0_550
	s_and_b32 s0, s90, 7
	s_lshl_b32 s0, s0, 3
	s_bfe_u32 s1, s90, 0x30003
	s_or_b32 s0, s0, s1
	s_andn2_b32 s20, s90, 63
	s_or_b32 s20, s20, s0
	v_readlane_b32 s0, v246, 32
	v_lshlrev_b32_e32 v13, 2, v6
	v_readlane_b32 s4, v246, 36
	v_readlane_b32 s5, v246, 37
	v_readlane_b32 s6, v246, 38
	v_readlane_b32 s7, v246, 39
	v_readlane_b32 s8, v246, 40
	v_readlane_b32 s9, v246, 41
	v_readlane_b32 s10, v246, 42
	v_readlane_b32 s11, v246, 43
	v_readlane_b32 s12, v246, 44
	v_readlane_b32 s13, v246, 45
	v_readlane_b32 s14, v246, 46
	v_readlane_b32 s15, v246, 47
	global_load_dword v16, v13, s[8:9]
	v_readlane_b32 s4, v246, 16
	v_readlane_b32 s1, v246, 33
	s_mul_i32 s0, s20, 0x3400
	v_readlane_b32 s6, v246, 18
	v_lshlrev_b32_e32 v14, 7, v4
	s_mul_hi_i32 s1, s20, 0x3400
	v_readlane_b32 s7, v246, 19
	s_add_u32 s0, s6, s0
	v_ashrrev_i32_e32 v15, 31, v14
	s_addc_u32 s1, s7, s1
	v_readlane_b32 s2, v246, 34
	v_lshl_add_u64 v[18:19], v[14:15], 1, s[0:1]
	v_lshlrev_b32_e32 v2, 1, v6
	v_mov_b32_e32 v3, 0
	v_lshl_add_u64 v[18:19], v[18:19], 0, v[2:3]
	s_mov_b64 s[6:7], 0x1b00
	s_movk_i32 s2, 0x1000
	v_lshl_add_u64 v[20:21], v[18:19], 0, s[6:7]
	v_add_co_u32_e32 v18, vcc, s2, v18
	v_readlane_b32 s12, v246, 24
	s_nop 0
	v_addc_co_u32_e32 v19, vcc, 0, v19, vcc
	global_load_ushort v30, v[20:21], off offset:2176
	global_load_ushort v23, v[18:19], off offset:2816
	global_load_ushort v24, v[20:21], off offset:2048
	global_load_ushort v31, v[20:21], off offset:128
	v_readlane_b32 s13, v246, 25
	v_readlane_b32 s14, v246, 26
	v_readlane_b32 s15, v246, 27
	v_lshlrev_b32_e32 v4, 1, v4
	v_max_f32_e32 v7, v7, v7
	v_max_f32_e32 v5, v5, v5
	v_max_f32_e32 v12, v12, v12
	v_max_f32_e32 v10, v10, v10
	s_waitcnt lgkmcnt(0)
	v_max_f32_e32 v11, v11, v11
	v_max_f32_e32 v8, v8, v8
	v_lshlrev_b32_e32 v18, 2, v9
	v_and_b32_e32 v19, 7, v9
	v_or_b32_e32 v22, 1, v4
	v_readlane_b32 s12, v248, 5
	v_readlane_b32 s3, v246, 35
	v_readlane_b32 s8, v246, 20
	v_readlane_b32 s9, v246, 21
	v_readlane_b32 s10, v246, 22
	v_readlane_b32 s18, v246, 30
	v_readlane_b32 s19, v246, 31
	s_movk_i32 s4, 0xc0
	v_max_f32_e32 v25, v5, v7
	v_max_f32_e32 v20, v10, v12
	v_max_f32_e32 v21, v8, v11
	v_and_b32_e32 v8, 32, v18
	v_lshlrev_b32_e32 v10, 1, v19
	v_mov_b32_e32 v11, v3
	v_readlane_b32 s13, v248, 6
	v_lshlrev_b32_e32 v12, 6, v22
	v_cmp_eq_u32_e64 s[0:1], 0, v6
	s_mov_b32 s8, 0x3c800000
	s_mov_b32 s3, 0x800000
	s_movk_i32 s9, 0x88
	s_mov_b32 s18, 0xf800000
	v_lshl_add_u64 v[6:7], s[54:55], 0, v[2:3]
	v_ashrrev_i32_e32 v5, 31, v4
	v_mul_f32_e32 v25, 0x41000000, v25
	v_and_or_b32 v8, v13, s4, v8
	v_lshl_add_u64 v[10:11], s[12:13], 0, v[10:11]
	s_lshl_b32 s10, s20, 4
	s_lshl_b32 s19, s96, 4
	v_lshlrev_b64 v[14:15], 1, v[14:15]
	v_ashrrev_i32_e32 v13, 31, v12
	v_mov_b32_e32 v27, 0x260

; #define NAP_LOAD(ROW) do { const bf16_t* pp_ = p.P + (size_t)(ROW) * L0LD + RWC + wave * 128 + lane; \
;         nq[0] = bf2f(pp_[0]); nq[1] = bf2f(pp_[64]); nk[0] = bf2f(pp_[1024]); nk[1] = bf2f(pp_[1088]); } while (0)
; __device__ __forceinline__ void ph_naprep(const Params& p, float* lds, int wg, int nwg) {
;     ...
;         const float qw = p.in[20][lane] * 0.125f, kw = p.in[21][lane];
;         float nq[2], nk[2];
;     ...
;         NAP_LOAD(wg < NT ? wg : 0);
	v_readlane_b32 s5, v246, 17
	v_readlane_b32 s11, v246, 23
	v_readlane_b32 s16, v246, 28
	v_readlane_b32 s17, v246, 29
	v_readlane_b32 s14, v248, 7
	v_readlane_b32 s15, v248, 8
	s_waitcnt vmcnt(4)
	v_mul_f32_e32 v26, 0x3e000000, v16
	v_mov_b32_e32 v16, 0x358637bd
	s_branch .LBB0_546
